# attn: A stores of the last 4 key tiles + final flush use sc1 (write-through) so less dirty L2 data remains at kernel end
# speedup vs baseline: 1.0295x; 1.0295x over previous
.Ll2f_top:
	ds_read_b128 v[98:101], v186 offset:18432
	ds_read_b128 v[162:165], v186 offset:18464
	ds_read_b128 v[194:197], v186 offset:27648
	ds_read_b128 v[198:201], v186 offset:27680
	ds_read_b128 v[202:205], v186 offset:18496
	ds_read_b128 v[206:209], v186 offset:18528
	ds_read_b128 v[210:213], v186 offset:27712
	ds_read_b128 v[166:169], v186 offset:27744
	s_nop 0
	v_exp_f32_e32 v215, v66
	v_exp_f32_e32 v217, v67
	v_exp_f32_e32 v219, v68
	v_exp_f32_e32 v221, v69
	v_exp_f32_e32 v223, v70
	v_exp_f32_e32 v71, v71
	v_exp_f32_e32 v225, v72
	v_exp_f32_e32 v227, v73
	v_exp_f32_e32 v229, v74
	v_exp_f32_e32 v231, v75
	s_waitcnt lgkmcnt(7)
	v_mfma_f32_32x32x16_f16 v[98:113], v[98:101], v[114:117], v[240:255]
	v_exp_f32_e32 v216, v82
	v_exp_f32_e32 v214, v83
	v_exp_f32_e32 v220, v84
	v_exp_f32_e32 v218, v85
	v_exp_f32_e32 v70, v86
	v_exp_f32_e32 v222, v87
	v_exp_f32_e32 v226, v88
	v_exp_f32_e32 v224, v89
	s_waitcnt lgkmcnt(6)
	v_mfma_f32_32x32x16_f16 v[98:113], v[162:165], v[118:121], v[98:113]
	v_exp_f32_e32 v233, v76
	v_exp_f32_e32 v235, v77
	v_exp_f32_e32 v230, v90
	v_exp_f32_e32 v228, v91
	v_exp_f32_e32 v234, v92
	v_exp_f32_e32 v232, v93
	v_exp_f32_e32 v237, v78
	v_exp_f32_e32 v236, v95
	s_waitcnt lgkmcnt(3)
	v_mfma_f32_32x32x16_f16 v[98:113], v[202:205], v[122:125], v[98:113]
	v_exp_f32_e32 v162, v94
	v_exp_f32_e32 v163, v79
	v_exp_f32_e32 v165, v80
	v_exp_f32_e32 v202, v96
	v_exp_f32_e32 v203, v81
	v_exp_f32_e32 v193, v97
	s_waitcnt lgkmcnt(2)
	v_mfma_f32_32x32x16_f16 v[98:113], v[206:209], v[126:129], v[98:113]
	s_waitcnt vmcnt(3)
	ds_write_b128 v185, v[146:149]
	s_waitcnt vmcnt(2)
	ds_write_b128 v185, v[150:153] offset:9216
	s_waitcnt vmcnt(1)
	ds_write_b128 v185, v[154:157] offset:55296
	s_waitcnt vmcnt(0)
	ds_write_b128 v185, v[158:161] offset:64512
	v_fma_f32 v150, v176, v216, v215
	v_fma_f32 v151, v176, v214, v217
	ds_read_b128 v[66:69], v189
	ds_read_b128 v[88:91], v189 offset:1152
	v_fma_f32 v152, v176, v220, v219
	v_fma_f32 v153, v176, v218, v221
	ds_read_b128 v[92:95], v189 offset:2304
	ds_read_b128 v[146:149], v189 offset:3456
	v_fma_f32 v154, v176, v70, v223
	v_fma_f32 v155, v176, v222, v71
	ds_write_b128 v190, v[150:153]
	v_fma_f32 v156, v176, v226, v225
	v_fma_f32 v157, v176, v224, v227
	ds_write_b128 v190, v[154:157] offset:16
	v_fma_f32 v158, v176, v230, v229
	v_fma_f32 v159, v176, v228, v231
	v_cvt_pk_f16_f32 v157, v156, v157
	v_fma_f32 v160, v176, v234, v233
	v_fma_f32 v161, v176, v232, v235
	ds_write_b128 v190, v[158:161] offset:64
	v_fma_f32 v162, v176, v162, v237
	v_fma_f32 v163, v176, v236, v163
	v_cvt_pk_f16_f32 v156, v154, v155
	v_fma_f32 v164, v176, v202, v165
	v_fma_f32 v165, v176, v193, v203
	ds_write_b128 v190, v[162:165] offset:80
	v_cvt_pk_f16_f32 v155, v152, v153
	v_cvt_pk_f16_f32 v154, v150, v151
	ds_read_b128 v[150:153], v191 offset:36864
	s_cmp_eq_u32 s19, 0
	s_cselect_b64 vcc, -1, 0
	s_add_i32 s20, s16, s1
	v_mfma_f32_32x32x16_f16 v[72:87], v[194:197], v[130:133], 0
	ds_read_b128 v[194:197], v191 offset:36896
	s_add_i32 s2, s20, 0x7c0
	s_and_b32 s2, s2, 0x7c0
	s_lshl_b32 s2, s2, 2
	v_lshl_add_u64 v[70:71], v[174:175], 0, s[2:3]
	v_cndmask_b32_e32 v71, v71, v179, vcc
	v_cndmask_b32_e32 v70, v70, v178, vcc
	s_waitcnt lgkmcnt(1)
	v_mfma_f32_32x32x16_f16 v[50:65], v[154:157], v[150:153], v[50:65]
	ds_read_b128 v[150:153], v191 offset:41472
	global_store_dwordx4 v[70:71], v[66:69], off nt
	ds_read_b128 v[66:69], v191 offset:41504
	v_cvt_pk_f16_f32 v165, v164, v165
	v_cvt_pk_f16_f32 v164, v162, v163
	v_cvt_pk_f16_f32 v163, v160, v161
	v_cvt_pk_f16_f32 v162, v158, v159
	s_waitcnt lgkmcnt(1)
	v_mfma_f32_32x32x16_f16 v[34:49], v[154:157], v[150:153], v[34:49]
	v_add_co_u32_e32 v96, vcc, s5, v70
	s_min_u32 s2, s19, 28
	s_nop 0
	v_addc_co_u32_e32 v97, vcc, 0, v71, vcc
	global_store_dwordx4 v[96:97], v[88:91], off nt
	s_add_i32 s21, s17, s2
	s_waitcnt lgkmcnt(0)
	v_mfma_f32_32x32x16_f16 v[34:49], v[162:165], v[66:69], v[34:49]
	ds_read_b128 v[66:69], v191 offset:46080
	v_add_co_u32_e32 v88, vcc, s13, v70
	s_lshl_b32 s2, s21, 13
	s_nop 0
	v_addc_co_u32_e32 v89, vcc, 0, v71, vcc
	global_store_dwordx4 v[88:89], v[92:95], off nt
	ds_read_b128 v[88:91], v191 offset:46112
	s_waitcnt lgkmcnt(1)
	v_mfma_f32_32x32x16_f16 v[18:33], v[154:157], v[66:69], v[18:33]
	v_add_co_u32_e32 v70, vcc, s14, v70
	s_and_b32 s2, s2, 0x3e000
	s_nop 0
	v_addc_co_u32_e32 v71, vcc, 0, v71, vcc
	v_lshl_add_u64 v[66:67], v[170:171], 0, s[2:3]
	v_add_co_u32_e32 v68, vcc, s15, v66
	global_store_dwordx4 v[70:71], v[146:149], off nt
	s_nop 0
	v_addc_co_u32_e32 v69, vcc, 0, v67, vcc
	s_waitcnt lgkmcnt(0)
	v_mfma_f32_32x32x16_f16 v[18:33], v[162:165], v[88:91], v[18:33]
	global_load_dwordx4 v[88:91], v[66:67], off
	global_load_dwordx4 v[92:95], v[68:69], off
	ds_read_b128 v[66:69], v191 offset:50688
	ds_read_b128 v[146:149], v191 offset:50720
	s_min_u32 s2, s19, 29
	s_add_i32 s2, s0, s2
	s_lshl_b32 s2, s2, 7
	s_and_b32 s2, s2, 0xf80
	s_waitcnt lgkmcnt(1)
	v_mfma_f32_32x32x16_f16 v[2:17], v[154:157], v[66:69], v[2:17]
	v_lshl_add_u64 v[66:67], v[172:173], 0, s[2:3]
	v_add_co_u32_e32 v68, vcc, s10, v66
	s_nop 0
	v_addc_co_u32_e32 v69, vcc, 0, v67, vcc
	global_load_dwordx4 v[150:153], v[66:67], off
	global_load_dwordx4 v[154:157], v[68:69], off
	v_mfma_f32_32x32x16_f16 v[72:87], v[198:201], v[134:137], v[72:87]
	v_exp_f32_e32 v97, v98
	s_waitcnt lgkmcnt(0)
	s_barrier
	v_mfma_f32_32x32x16_f16 v[72:87], v[210:213], v[138:141], v[72:87]
	v_mfma_f32_32x32x16_f16 v[72:87], v[166:169], v[142:145], v[72:87]
	v_mfma_f32_32x32x16_f16 v[50:65], v[162:165], v[194:197], v[50:65]
	s_nop 0
	ds_read_b128 v[66:69], v186
	ds_read_b128 v[158:161], v186 offset:32
	ds_read_b128 v[194:197], v186 offset:9216
	ds_read_b128 v[198:201], v186 offset:9248
	ds_read_b128 v[202:205], v186 offset:64
	ds_read_b128 v[206:209], v186 offset:96
	v_exp_f32_e32 v167, v99
	v_exp_f32_e32 v99, v100
	v_exp_f32_e32 v169, v101
	v_exp_f32_e32 v101, v102
	v_mfma_f32_32x32x16_f16 v[2:17], v[162:165], v[146:149], v[2:17]
	ds_read_b128 v[146:149], v186 offset:9280
	ds_read_b128 v[162:165], v186 offset:9312
	v_exp_f32_e32 v211, v103
	v_exp_f32_e32 v103, v104
	v_exp_f32_e32 v213, v105
	v_exp_f32_e32 v105, v106
	v_exp_f32_e32 v215, v107
	v_exp_f32_e32 v107, v108
	v_exp_f32_e32 v217, v109
	v_exp_f32_e32 v166, v72
	v_exp_f32_e32 v96, v73
	v_exp_f32_e32 v168, v74
	v_exp_f32_e32 v98, v75
	v_exp_f32_e32 v210, v76
	v_exp_f32_e32 v100, v77
	v_exp_f32_e32 v212, v78
	v_exp_f32_e32 v102, v79
	v_exp_f32_e32 v214, v80
	v_exp_f32_e32 v104, v81
	s_waitcnt lgkmcnt(7)
	v_mfma_f32_32x32x16_f16 v[66:81], v[66:69], v[114:117], v[240:255]
	v_exp_f32_e32 v109, v110
	v_exp_f32_e32 v216, v82
	v_exp_f32_e32 v106, v83
	v_exp_f32_e32 v219, v111
	s_waitcnt lgkmcnt(6)
	v_mfma_f32_32x32x16_f16 v[66:81], v[158:161], v[118:121], v[66:81]
	v_exp_f32_e32 v218, v84
	v_exp_f32_e32 v108, v85
	v_exp_f32_e32 v111, v112
	v_exp_f32_e32 v110, v87
	s_waitcnt lgkmcnt(3)
	v_mfma_f32_32x32x16_f16 v[66:81], v[202:205], v[122:125], v[66:81]
	v_exp_f32_e32 v202, v86
	v_exp_f32_e32 v203, v113
	s_waitcnt lgkmcnt(2)
	v_mfma_f32_32x32x16_f16 v[66:81], v[206:209], v[126:129], v[66:81]
	s_waitcnt vmcnt(3)
	ds_write_b128 v185, v[88:91] offset:18432
	s_waitcnt vmcnt(2)
	ds_write_b128 v185, v[92:95] offset:27648
	s_waitcnt vmcnt(1)
	ds_write_b128 v185, v[150:153] offset:36864
	s_waitcnt vmcnt(0)
	ds_write_b128 v185, v[154:157] offset:46080
	v_fma_f32 v150, v176, v166, v97
	v_fma_f32 v151, v176, v96, v167
	v_mfma_f32_32x32x16_f16 v[82:97], v[194:197], v[130:133], 0
	v_fma_f32 v152, v176, v168, v99
	v_fma_f32 v153, v176, v98, v169
	v_fma_f32 v154, v176, v210, v101
	v_fma_f32 v155, v176, v100, v211
	v_fma_f32 v156, v176, v212, v103
	v_fma_f32 v157, v176, v102, v213
	v_fma_f32 v158, v176, v214, v105
	v_fma_f32 v159, v176, v104, v215
	v_fma_f32 v160, v176, v216, v107
	v_fma_f32 v161, v176, v106, v217
	v_fma_f32 v166, v176, v218, v109
	v_fma_f32 v167, v176, v108, v219
	v_fma_f32 v168, v176, v202, v111
	v_fma_f32 v169, v176, v110, v203
	ds_read_b128 v[98:101], v189
	ds_read_b128 v[102:105], v189 offset:1152
	ds_read_b128 v[106:109], v189 offset:2304
	ds_read_b128 v[110:113], v189 offset:3456
	ds_write_b128 v190, v[150:153]
	ds_write_b128 v190, v[154:157] offset:16
	ds_write_b128 v190, v[158:161] offset:64
	ds_write_b128 v190, v[166:169] offset:80
	v_cvt_pk_f16_f32 v157, v156, v157
	v_cvt_pk_f16_f32 v156, v154, v155
	v_cvt_pk_f16_f32 v155, v152, v153
	v_cvt_pk_f16_f32 v154, v150, v151
	ds_read_b128 v[150:153], v191 offset:55296
	ds_read_b128 v[194:197], v191 offset:55328
	v_mfma_f32_32x32x16_f16 v[82:97], v[198:201], v[134:137], v[82:97]
	s_and_b32 s2, s20, 0x7c0
	s_min_u32 s20, s19, 27
	s_lshl_b32 s2, s2, 2
	s_add_i32 s20, s18, s20
	v_lshl_add_u64 v[210:211], v[174:175], 0, s[2:3]
	s_lshl_b32 s2, s20, 13
	s_and_b32 s2, s2, 0x3e000
	s_waitcnt lgkmcnt(1)
	v_mfma_f32_32x32x16_f16 v[50:65], v[154:157], v[150:153], v[50:65]
	ds_read_b128 v[150:153], v191 offset:59904
	ds_read_b128 v[198:201], v191 offset:59936
	s_lshl_b32 s21, s21, 7
	v_cvt_pk_f16_f32 v169, v168, v169
	v_cvt_pk_f16_f32 v168, v166, v167
	v_cvt_pk_f16_f32 v166, v158, v159
	v_cvt_pk_f16_f32 v167, v160, v161
	s_addk_i32 s1, 0x80
	s_waitcnt lgkmcnt(1)
	v_mfma_f32_32x32x16_f16 v[34:49], v[154:157], v[150:153], v[34:49]
	ds_read_b128 v[150:153], v191 offset:64512
	ds_read_b128 v[202:205], v191 offset:64544
	s_waitcnt lgkmcnt(1)
	v_mfma_f32_32x32x16_f16 v[18:33], v[154:157], v[150:153], v[18:33]
	ds_read_b128 v[150:153], v192 offset:13824
	ds_read_b128 v[206:209], v192 offset:13856
	v_mfma_f32_32x32x16_f16 v[82:97], v[146:149], v[138:141], v[82:97]
	v_lshl_add_u64 v[146:147], v[170:171], 0, s[2:3]
	s_and_b32 s2, s21, 0xf80
	v_lshl_add_u64 v[158:159], v[172:173], 0, s[2:3]
	s_add_i32 s2, s19, 2
	s_cmp_lt_u32 s19, 26
	s_mov_b32 s19, s2
	s_waitcnt lgkmcnt(1)
	v_mfma_f32_32x32x16_f16 v[2:17], v[154:157], v[150:153], v[2:17]
	v_add_co_u32_e32 v150, vcc, s15, v146
	s_nop 1
	v_addc_co_u32_e32 v151, vcc, 0, v147, vcc
	global_load_dwordx4 v[146:149], v[146:147], off
	s_nop 0
	global_load_dwordx4 v[150:153], v[150:151], off
	s_nop 0
	global_load_dwordx4 v[154:157], v[158:159], off
	v_add_co_u32_e32 v158, vcc, s10, v158
	v_mfma_f32_32x32x16_f16 v[50:65], v[166:169], v[194:197], v[50:65]
	s_nop 0
	v_addc_co_u32_e32 v159, vcc, 0, v159, vcc
	global_load_dwordx4 v[158:161], v[158:159], off
	v_add_co_u32_e32 v194, vcc, s5, v210
	s_nop 1
	v_addc_co_u32_e32 v195, vcc, 0, v211, vcc
	v_mfma_f32_32x32x16_f16 v[34:49], v[166:169], v[198:201], v[34:49]
	v_add_co_u32_e32 v196, vcc, s13, v210
	s_nop 1
	v_addc_co_u32_e32 v197, vcc, 0, v211, vcc
	v_mfma_f32_32x32x16_f16 v[18:33], v[166:169], v[202:205], v[18:33]
	s_waitcnt lgkmcnt(0)
	v_mfma_f32_32x32x16_f16 v[2:17], v[166:169], v[206:209], v[2:17]
	v_add_co_u32_e32 v166, vcc, s14, v210
	s_nop 1
	v_addc_co_u32_e32 v167, vcc, 0, v211, vcc
	global_store_dwordx4 v[210:211], v[98:101], off nt
	global_store_dwordx4 v[194:195], v[102:105], off nt
	global_store_dwordx4 v[196:197], v[106:109], off nt
	global_store_dwordx4 v[166:167], v[110:113], off nt
	v_mfma_f32_32x32x16_f16 v[82:97], v[162:165], v[142:145], v[82:97]
	s_barrier
	s_cbranch_scc1 .Ll2f_top
	.p2alignl 6, 3212836864
	s_nop 0
	s_nop 0
	s_nop 0
	s_nop 0
.Ll2t_top:
	ds_read_b128 v[98:101], v186 offset:18432
	ds_read_b128 v[162:165], v186 offset:18464
	ds_read_b128 v[194:197], v186 offset:27648
	ds_read_b128 v[198:201], v186 offset:27680
	ds_read_b128 v[202:205], v186 offset:18496
	ds_read_b128 v[206:209], v186 offset:18528
	ds_read_b128 v[210:213], v186 offset:27712
	ds_read_b128 v[166:169], v186 offset:27744
	s_nop 0
	v_exp_f32_e32 v215, v66
	v_exp_f32_e32 v217, v67
	v_exp_f32_e32 v219, v68
	v_exp_f32_e32 v221, v69
	v_exp_f32_e32 v223, v70
	v_exp_f32_e32 v71, v71
	v_exp_f32_e32 v225, v72
	v_exp_f32_e32 v227, v73
	v_exp_f32_e32 v229, v74
	v_exp_f32_e32 v231, v75
	s_waitcnt lgkmcnt(7)
	v_mfma_f32_32x32x16_f16 v[98:113], v[98:101], v[114:117], v[240:255]
	v_exp_f32_e32 v216, v82
	v_exp_f32_e32 v214, v83
	v_exp_f32_e32 v220, v84
	v_exp_f32_e32 v218, v85
	v_exp_f32_e32 v70, v86
	v_exp_f32_e32 v222, v87
	v_exp_f32_e32 v226, v88
	v_exp_f32_e32 v224, v89
	s_waitcnt lgkmcnt(6)
	v_mfma_f32_32x32x16_f16 v[98:113], v[162:165], v[118:121], v[98:113]
	v_exp_f32_e32 v233, v76
	v_exp_f32_e32 v235, v77
	v_exp_f32_e32 v230, v90
	v_exp_f32_e32 v228, v91
	v_exp_f32_e32 v234, v92
	v_exp_f32_e32 v232, v93
	v_exp_f32_e32 v237, v78
	v_exp_f32_e32 v236, v95
	s_waitcnt lgkmcnt(3)
	v_mfma_f32_32x32x16_f16 v[98:113], v[202:205], v[122:125], v[98:113]
	v_exp_f32_e32 v162, v94
	v_exp_f32_e32 v163, v79
	v_exp_f32_e32 v165, v80
	v_exp_f32_e32 v202, v96
	v_exp_f32_e32 v203, v81
	v_exp_f32_e32 v193, v97
	s_waitcnt lgkmcnt(2)
	v_mfma_f32_32x32x16_f16 v[98:113], v[206:209], v[126:129], v[98:113]
	s_waitcnt vmcnt(3)
	ds_write_b128 v185, v[146:149]
	s_waitcnt vmcnt(2)
	ds_write_b128 v185, v[150:153] offset:9216
	s_waitcnt vmcnt(1)
	ds_write_b128 v185, v[154:157] offset:55296
	s_waitcnt vmcnt(0)
	ds_write_b128 v185, v[158:161] offset:64512
	v_fma_f32 v150, v176, v216, v215
	v_fma_f32 v151, v176, v214, v217
	ds_read_b128 v[66:69], v189
	ds_read_b128 v[88:91], v189 offset:1152
	v_fma_f32 v152, v176, v220, v219
	v_fma_f32 v153, v176, v218, v221
	ds_read_b128 v[92:95], v189 offset:2304
	ds_read_b128 v[146:149], v189 offset:3456
	v_fma_f32 v154, v176, v70, v223
	v_fma_f32 v155, v176, v222, v71
	ds_write_b128 v190, v[150:153]
	v_fma_f32 v156, v176, v226, v225
	v_fma_f32 v157, v176, v224, v227
	ds_write_b128 v190, v[154:157] offset:16
	v_fma_f32 v158, v176, v230, v229
	v_fma_f32 v159, v176, v228, v231
	v_cvt_pk_f16_f32 v157, v156, v157
	v_fma_f32 v160, v176, v234, v233
	v_fma_f32 v161, v176, v232, v235
	ds_write_b128 v190, v[158:161] offset:64
	v_fma_f32 v162, v176, v162, v237
	v_fma_f32 v163, v176, v236, v163
	v_cvt_pk_f16_f32 v156, v154, v155
	v_fma_f32 v164, v176, v202, v165
	v_fma_f32 v165, v176, v193, v203
	ds_write_b128 v190, v[162:165] offset:80
	v_cvt_pk_f16_f32 v155, v152, v153
	v_cvt_pk_f16_f32 v154, v150, v151
	ds_read_b128 v[150:153], v191 offset:36864
	s_cmp_eq_u32 s19, 0
	s_cselect_b64 vcc, -1, 0
	s_add_i32 s20, s16, s1
	v_mfma_f32_32x32x16_f16 v[72:87], v[194:197], v[130:133], 0
	ds_read_b128 v[194:197], v191 offset:36896
	s_add_i32 s2, s20, 0x7c0
	s_and_b32 s2, s2, 0x7c0
	s_lshl_b32 s2, s2, 2
	v_lshl_add_u64 v[70:71], v[174:175], 0, s[2:3]
	v_cndmask_b32_e32 v71, v71, v179, vcc
	v_cndmask_b32_e32 v70, v70, v178, vcc
	s_waitcnt lgkmcnt(1)
	v_mfma_f32_32x32x16_f16 v[50:65], v[154:157], v[150:153], v[50:65]
	ds_read_b128 v[150:153], v191 offset:41472
	global_store_dwordx4 v[70:71], v[66:69], off sc1
	ds_read_b128 v[66:69], v191 offset:41504
	v_cvt_pk_f16_f32 v165, v164, v165
	v_cvt_pk_f16_f32 v164, v162, v163
	v_cvt_pk_f16_f32 v163, v160, v161
	v_cvt_pk_f16_f32 v162, v158, v159
	s_waitcnt lgkmcnt(1)
	v_mfma_f32_32x32x16_f16 v[34:49], v[154:157], v[150:153], v[34:49]
	v_add_co_u32_e32 v96, vcc, s5, v70
	s_min_u32 s2, s19, 28
	s_nop 0
	v_addc_co_u32_e32 v97, vcc, 0, v71, vcc
	global_store_dwordx4 v[96:97], v[88:91], off sc1
	s_add_i32 s21, s17, s2
	s_waitcnt lgkmcnt(0)
	v_mfma_f32_32x32x16_f16 v[34:49], v[162:165], v[66:69], v[34:49]
	ds_read_b128 v[66:69], v191 offset:46080
	v_add_co_u32_e32 v88, vcc, s13, v70
	s_lshl_b32 s2, s21, 13
	s_nop 0
	v_addc_co_u32_e32 v89, vcc, 0, v71, vcc
	global_store_dwordx4 v[88:89], v[92:95], off sc1
	ds_read_b128 v[88:91], v191 offset:46112
	s_waitcnt lgkmcnt(1)
	v_mfma_f32_32x32x16_f16 v[18:33], v[154:157], v[66:69], v[18:33]
	v_add_co_u32_e32 v70, vcc, s14, v70
	s_and_b32 s2, s2, 0x3e000
	s_nop 0
	v_addc_co_u32_e32 v71, vcc, 0, v71, vcc
	v_lshl_add_u64 v[66:67], v[170:171], 0, s[2:3]
	v_add_co_u32_e32 v68, vcc, s15, v66
	global_store_dwordx4 v[70:71], v[146:149], off sc1
	s_nop 0
	v_addc_co_u32_e32 v69, vcc, 0, v67, vcc
	s_waitcnt lgkmcnt(0)
	v_mfma_f32_32x32x16_f16 v[18:33], v[162:165], v[88:91], v[18:33]
	global_load_dwordx4 v[88:91], v[66:67], off
	global_load_dwordx4 v[92:95], v[68:69], off
	ds_read_b128 v[66:69], v191 offset:50688
	ds_read_b128 v[146:149], v191 offset:50720
	s_min_u32 s2, s19, 29
	s_add_i32 s2, s0, s2
	s_lshl_b32 s2, s2, 7
	s_and_b32 s2, s2, 0xf80
	s_waitcnt lgkmcnt(1)
	v_mfma_f32_32x32x16_f16 v[2:17], v[154:157], v[66:69], v[2:17]
	v_lshl_add_u64 v[66:67], v[172:173], 0, s[2:3]
	v_add_co_u32_e32 v68, vcc, s10, v66
	s_nop 0
	v_addc_co_u32_e32 v69, vcc, 0, v67, vcc
	global_load_dwordx4 v[150:153], v[66:67], off
	global_load_dwordx4 v[154:157], v[68:69], off
	v_mfma_f32_32x32x16_f16 v[72:87], v[198:201], v[134:137], v[72:87]
	v_exp_f32_e32 v97, v98
	s_waitcnt lgkmcnt(0)
	s_barrier
	v_mfma_f32_32x32x16_f16 v[72:87], v[210:213], v[138:141], v[72:87]
	v_mfma_f32_32x32x16_f16 v[72:87], v[166:169], v[142:145], v[72:87]
	v_mfma_f32_32x32x16_f16 v[50:65], v[162:165], v[194:197], v[50:65]
	s_nop 0
	ds_read_b128 v[66:69], v186
	ds_read_b128 v[158:161], v186 offset:32
	ds_read_b128 v[194:197], v186 offset:9216
	ds_read_b128 v[198:201], v186 offset:9248
	ds_read_b128 v[202:205], v186 offset:64
	ds_read_b128 v[206:209], v186 offset:96
	v_exp_f32_e32 v167, v99
	v_exp_f32_e32 v99, v100
	v_exp_f32_e32 v169, v101
	v_exp_f32_e32 v101, v102
	v_mfma_f32_32x32x16_f16 v[2:17], v[162:165], v[146:149], v[2:17]
	ds_read_b128 v[146:149], v186 offset:9280
	ds_read_b128 v[162:165], v186 offset:9312
	v_exp_f32_e32 v211, v103
	v_exp_f32_e32 v103, v104
	v_exp_f32_e32 v213, v105
	v_exp_f32_e32 v105, v106
	v_exp_f32_e32 v215, v107
	v_exp_f32_e32 v107, v108
	v_exp_f32_e32 v217, v109
	v_exp_f32_e32 v166, v72
	v_exp_f32_e32 v96, v73
	v_exp_f32_e32 v168, v74
	v_exp_f32_e32 v98, v75
	v_exp_f32_e32 v210, v76
	v_exp_f32_e32 v100, v77
	v_exp_f32_e32 v212, v78
	v_exp_f32_e32 v102, v79
	v_exp_f32_e32 v214, v80
	v_exp_f32_e32 v104, v81
	s_waitcnt lgkmcnt(7)
	v_mfma_f32_32x32x16_f16 v[66:81], v[66:69], v[114:117], v[240:255]
	v_exp_f32_e32 v109, v110
	v_exp_f32_e32 v216, v82
	v_exp_f32_e32 v106, v83
	v_exp_f32_e32 v219, v111
	s_waitcnt lgkmcnt(6)
	v_mfma_f32_32x32x16_f16 v[66:81], v[158:161], v[118:121], v[66:81]
	v_exp_f32_e32 v218, v84
	v_exp_f32_e32 v108, v85
	v_exp_f32_e32 v111, v112
	v_exp_f32_e32 v110, v87
	s_waitcnt lgkmcnt(3)
	v_mfma_f32_32x32x16_f16 v[66:81], v[202:205], v[122:125], v[66:81]
	v_exp_f32_e32 v202, v86
	v_exp_f32_e32 v203, v113
	s_waitcnt lgkmcnt(2)
	v_mfma_f32_32x32x16_f16 v[66:81], v[206:209], v[126:129], v[66:81]
	s_waitcnt vmcnt(3)
	ds_write_b128 v185, v[88:91] offset:18432
	s_waitcnt vmcnt(2)
	ds_write_b128 v185, v[92:95] offset:27648
	s_waitcnt vmcnt(1)
	ds_write_b128 v185, v[150:153] offset:36864
	s_waitcnt vmcnt(0)
	ds_write_b128 v185, v[154:157] offset:46080
	v_fma_f32 v150, v176, v166, v97
	v_fma_f32 v151, v176, v96, v167
	v_mfma_f32_32x32x16_f16 v[82:97], v[194:197], v[130:133], 0
	v_fma_f32 v152, v176, v168, v99
	v_fma_f32 v153, v176, v98, v169
	v_fma_f32 v154, v176, v210, v101
	v_fma_f32 v155, v176, v100, v211
	v_fma_f32 v156, v176, v212, v103
	v_fma_f32 v157, v176, v102, v213
	v_fma_f32 v158, v176, v214, v105
	v_fma_f32 v159, v176, v104, v215
	v_fma_f32 v160, v176, v216, v107
	v_fma_f32 v161, v176, v106, v217
	v_fma_f32 v166, v176, v218, v109
	v_fma_f32 v167, v176, v108, v219
	v_fma_f32 v168, v176, v202, v111
	v_fma_f32 v169, v176, v110, v203
	ds_read_b128 v[98:101], v189
	ds_read_b128 v[102:105], v189 offset:1152
	ds_read_b128 v[106:109], v189 offset:2304
	ds_read_b128 v[110:113], v189 offset:3456
	ds_write_b128 v190, v[150:153]
	ds_write_b128 v190, v[154:157] offset:16
	ds_write_b128 v190, v[158:161] offset:64
	ds_write_b128 v190, v[166:169] offset:80
	v_cvt_pk_f16_f32 v157, v156, v157
	v_cvt_pk_f16_f32 v156, v154, v155
	v_cvt_pk_f16_f32 v155, v152, v153
	v_cvt_pk_f16_f32 v154, v150, v151
	ds_read_b128 v[150:153], v191 offset:55296
	ds_read_b128 v[194:197], v191 offset:55328
	v_mfma_f32_32x32x16_f16 v[82:97], v[198:201], v[134:137], v[82:97]
	s_and_b32 s2, s20, 0x7c0
	s_min_u32 s20, s19, 27
	s_lshl_b32 s2, s2, 2
	s_add_i32 s20, s18, s20
	v_lshl_add_u64 v[210:211], v[174:175], 0, s[2:3]
	s_lshl_b32 s2, s20, 13
	s_and_b32 s2, s2, 0x3e000
	s_waitcnt lgkmcnt(1)
	v_mfma_f32_32x32x16_f16 v[50:65], v[154:157], v[150:153], v[50:65]
	ds_read_b128 v[150:153], v191 offset:59904
	ds_read_b128 v[198:201], v191 offset:59936
	s_lshl_b32 s21, s21, 7
	v_cvt_pk_f16_f32 v169, v168, v169
	v_cvt_pk_f16_f32 v168, v166, v167
	v_cvt_pk_f16_f32 v166, v158, v159
	v_cvt_pk_f16_f32 v167, v160, v161
	s_addk_i32 s1, 0x80
	s_waitcnt lgkmcnt(1)
	v_mfma_f32_32x32x16_f16 v[34:49], v[154:157], v[150:153], v[34:49]
	ds_read_b128 v[150:153], v191 offset:64512
	ds_read_b128 v[202:205], v191 offset:64544
	s_waitcnt lgkmcnt(1)
	v_mfma_f32_32x32x16_f16 v[18:33], v[154:157], v[150:153], v[18:33]
	ds_read_b128 v[150:153], v192 offset:13824
	ds_read_b128 v[206:209], v192 offset:13856
	v_mfma_f32_32x32x16_f16 v[82:97], v[146:149], v[138:141], v[82:97]
	v_lshl_add_u64 v[146:147], v[170:171], 0, s[2:3]
	s_and_b32 s2, s21, 0xf80
	v_lshl_add_u64 v[158:159], v[172:173], 0, s[2:3]
	s_add_i32 s2, s19, 2
	s_cmp_lt_u32 s19, 30
	s_mov_b32 s19, s2
	s_waitcnt lgkmcnt(1)
	v_mfma_f32_32x32x16_f16 v[2:17], v[154:157], v[150:153], v[2:17]
	v_add_co_u32_e32 v150, vcc, s15, v146
	s_nop 1
	v_addc_co_u32_e32 v151, vcc, 0, v147, vcc
	global_load_dwordx4 v[146:149], v[146:147], off
	s_nop 0
	global_load_dwordx4 v[150:153], v[150:151], off
	s_nop 0
	global_load_dwordx4 v[154:157], v[158:159], off
	v_add_co_u32_e32 v158, vcc, s10, v158
	v_mfma_f32_32x32x16_f16 v[50:65], v[166:169], v[194:197], v[50:65]
	s_nop 0
	v_addc_co_u32_e32 v159, vcc, 0, v159, vcc
	global_load_dwordx4 v[158:161], v[158:159], off
	v_add_co_u32_e32 v194, vcc, s5, v210
	s_nop 1
	v_addc_co_u32_e32 v195, vcc, 0, v211, vcc
	v_mfma_f32_32x32x16_f16 v[34:49], v[166:169], v[198:201], v[34:49]
	v_add_co_u32_e32 v196, vcc, s13, v210
	s_nop 1
	v_addc_co_u32_e32 v197, vcc, 0, v211, vcc
	v_mfma_f32_32x32x16_f16 v[18:33], v[166:169], v[202:205], v[18:33]
	s_waitcnt lgkmcnt(0)
	v_mfma_f32_32x32x16_f16 v[2:17], v[166:169], v[206:209], v[2:17]
	v_add_co_u32_e32 v166, vcc, s14, v210
	s_nop 1
	v_addc_co_u32_e32 v167, vcc, 0, v211, vcc
	global_store_dwordx4 v[210:211], v[98:101], off sc1
	global_store_dwordx4 v[194:195], v[102:105], off sc1
	global_store_dwordx4 v[196:197], v[106:109], off sc1
	global_store_dwordx4 v[166:167], v[110:113], off sc1
	v_mfma_f32_32x32x16_f16 v[82:97], v[162:165], v[142:145], v[82:97]
	s_barrier
	s_cbranch_scc1 .Ll2t_top
.Ll2_post:
	ds_read_b128 v[66:69], v189
	ds_read_b128 v[70:73], v189 offset:1152
	s_addk_i32 s11, 0x7c0
	s_and_b32 s0, s11, 0x7c0
	s_lshl_b32 s0, s0, 2
	s_mov_b32 s1, 0
	v_lshl_add_u64 v[74:75], v[174:175], 0, s[0:1]
	s_waitcnt lgkmcnt(1)
	global_store_dwordx4 v[74:75], v[66:69], off sc1
	s_mov_b32 s0, 0x10800
	v_lshlrev_b32_e32 v1, 2, v1
	v_add_co_u32_e32 v66, vcc, 0x10000, v74
	v_lshrrev_b32_e32 v86, 2, v0
	s_nop 0
	v_addc_co_u32_e32 v67, vcc, 0, v75, vcc
	s_waitcnt lgkmcnt(0)
	global_store_dwordx4 v[66:67], v[70:73], off sc1
	ds_read_b128 v[66:69], v189 offset:2304
	ds_read_b128 v[70:73], v189 offset:3456
	v_add_co_u32_e32 v76, vcc, 0x20000, v74
	v_lshlrev_b32_e32 v0, 5, v0
	s_nop 0
	v_addc_co_u32_e32 v77, vcc, 0, v75, vcc
	s_waitcnt lgkmcnt(1)
	global_store_dwordx4 v[76:77], v[66:69], off sc1
	v_and_b32_e32 v87, 0x60, v0
	v_lshlrev_b32_e32 v88, 2, v87
	v_add_co_u32_e32 v66, vcc, 0x30000, v74
	s_nop 1
	v_addc_co_u32_e32 v67, vcc, 0, v75, vcc
	s_waitcnt lgkmcnt(0)
	global_store_dwordx4 v[66:67], v[70:73], off sc1
	v_lshl_or_b32 v67, v182, 2, v183
	v_mad_u32_u24 v66, v184, s0, 0
	v_mul_u32_u24_e32 v67, 0x210, v67
	v_add3_u32 v1, v66, v1, v67
	s_barrier
	ds_write2_b32 v1, v50, v34 offset1:32
	ds_write2_b32 v1, v51, v35 offset0:132 offset1:164
	v_add_u32_e32 v34, 0x400, v1
	ds_write2_b32 v34, v52, v36 offset0:8 offset1:40
	ds_write2_b32 v34, v53, v37 offset0:140 offset1:172
	v_add_u32_e32 v35, 0x1000, v1
	v_add_u32_e32 v36, 0x1400, v1
	ds_write2_b32 v35, v54, v38 offset0:32 offset1:64
	ds_write2_b32 v35, v55, v39 offset0:164 offset1:196
	ds_write2_b32 v36, v56, v40 offset0:40 offset1:72
	ds_write2_b32 v36, v57, v41 offset0:172 offset1:204
	v_add_u32_e32 v37, 0x2000, v1
	v_add_u32_e32 v38, 0x2400, v1
	v_add_u32_e32 v40, 0x3200, v1
	ds_write2_b32 v37, v58, v42 offset0:64 offset1:96
	ds_write2_b32 v37, v59, v43 offset0:196 offset1:228
	ds_write2_b32 v38, v60, v44 offset0:72 offset1:104
	ds_write2_b32 v38, v61, v45 offset0:204 offset1:236
	v_add_u32_e32 v39, 0x3000, v1
	ds_write2_b32 v40, v63, v47 offset0:100 offset1:132
	v_add_u32_e32 v40, 0x3400, v1
	v_add_u32_e32 v41, 0x3600, v1
	ds_write2_b32 v39, v62, v46 offset0:96 offset1:128
	ds_write2_b32 v40, v64, v48 offset0:104 offset1:136
	ds_write2_b32 v41, v65, v49 offset0:108 offset1:140
	ds_write2_b32 v1, v18, v2 offset0:64 offset1:96
	ds_write2_b32 v1, v19, v3 offset0:196 offset1:228
	ds_write2_b32 v34, v20, v4 offset0:72 offset1:104
	ds_write2_b32 v34, v21, v5 offset0:204 offset1:236
	ds_write2_b32 v35, v22, v6 offset0:96 offset1:128
	v_add_u32_e32 v2, 0x1200, v1
	ds_write2_b32 v2, v23, v7 offset0:100 offset1:132
	ds_write2_b32 v36, v24, v8 offset0:104 offset1:136
	v_add_u32_e32 v2, 0x1600, v1
	ds_write2_b32 v2, v25, v9 offset0:108 offset1:140
	ds_write2_b32 v37, v26, v10 offset0:128 offset1:160
	ds_write2_b32 v38, v27, v11 offset0:4 offset1:36
	ds_write2_b32 v38, v28, v12 offset0:136 offset1:168
	v_add_u32_e32 v2, 0x2800, v1
	v_add_u32_e32 v1, 0x3800, v1
	ds_write2_b32 v2, v29, v13 offset0:12 offset1:44
	ds_write2_b32 v39, v30, v14 offset0:160 offset1:192
	ds_write2_b32 v40, v31, v15 offset0:36 offset1:68
	ds_write2_b32 v40, v32, v16 offset0:168 offset1:200
	ds_write2_b32 v1, v33, v17 offset0:44 offset1:76
	v_mul_u32_u24_e32 v1, 0x210, v86
	v_add3_u32 v89, 0, v1, v88
	v_add_u32_e32 v0, 0x10800, v89
	s_waitcnt lgkmcnt(0)
	s_barrier
	ds_read_b128 v[10:13], v0
	ds_read_b128 v[14:17], v0 offset:16
	ds_read_b128 v[4:7], v89 offset:16
	ds_read_b128 v[18:21], v89
	v_add_u32_e32 v26, 0x10820, v89
	ds_read_b128 v[22:25], v89 offset:32
	ds_read_b128 v[0:3], v89 offset:48
	v_add_u32_e32 v34, 0x10810, v89
	s_waitcnt lgkmcnt(3)
	v_pk_add_f32 v[16:17], v[6:7], v[16:17]
	v_pk_add_f32 v[14:15], v[4:5], v[14:15]
	s_waitcnt lgkmcnt(2)
	v_pk_add_f32 v[10:11], v[18:19], v[10:11]
	v_pk_add_f32 v[8:9], v[20:21], v[12:13]
	v_pk_mul_f32 v[20:21], v[16:17], v[16:17]
	v_pk_mul_f32 v[16:17], v[10:11], v[10:11]
	v_pk_mul_f32 v[14:15], v[14:15], v[14:15]
	v_pk_mul_f32 v[12:13], v[8:9], v[8:9]
	v_mov_b32_e32 v18, v16
	v_mov_b32_e32 v19, v14
	v_mov_b32_e32 v14, v17
	v_pk_add_f32 v[14:15], v[18:19], v[14:15]
	v_mov_b32_e32 v16, v12
	v_mov_b32_e32 v17, v20
	v_pk_add_f32 v[18:19], v[14:15], v[16:17]
	v_mov_b32_e32 v20, v13
	ds_read_b128 v[14:17], v26 offset:16
	v_pk_add_f32 v[12:13], v[18:19], v[20:21]
	ds_read_b128 v[18:21], v26
	v_add_u32_e32 v38, 0x10840, v89
	ds_read_b128 v[26:29], v38
	s_waitcnt lgkmcnt(2)
	v_pk_add_f32 v[32:33], v[0:1], v[14:15]
	v_pk_add_f32 v[30:31], v[2:3], v[16:17]
	s_waitcnt lgkmcnt(1)
	v_pk_add_f32 v[80:81], v[22:23], v[18:19]
	v_pk_add_f32 v[78:79], v[24:25], v[20:21]
	v_pk_mul_f32 v[18:19], v[80:81], v[80:81]
	v_pk_mul_f32 v[22:23], v[32:33], v[32:33]
	v_pk_mul_f32 v[20:21], v[78:79], v[78:79]
	v_pk_mul_f32 v[30:31], v[30:31], v[30:31]
	v_mov_b32_e32 v24, v18
	v_mov_b32_e32 v25, v22
	v_mov_b32_e32 v22, v19
	v_pk_add_f32 v[18:19], v[24:25], v[22:23]
	v_mov_b32_e32 v22, v20
	v_mov_b32_e32 v23, v30
	ds_read_b128 v[14:17], v34
	v_pk_add_f32 v[32:33], v[18:19], v[22:23]
	v_mov_b32_e32 v30, v21
	ds_read_b128 v[18:21], v89 offset:80
	ds_read_b128 v[22:25], v38 offset:16
	v_pk_add_f32 v[82:83], v[32:33], v[30:31]
	ds_read_b128 v[30:33], v89 offset:64
	ds_read_b128 v[34:37], v89 offset:80
	ds_read_b128 v[38:41], v38
	ds_read_b128 v[42:45], v89 offset:64
	v_add_u32_e32 v74, 0x10860, v89
	s_waitcnt lgkmcnt(4)
	v_pk_add_f32 v[20:21], v[20:21], v[24:25]
	v_pk_add_f32 v[18:19], v[18:19], v[22:23]
	s_waitcnt lgkmcnt(3)
	v_pk_add_f32 v[22:23], v[30:31], v[26:27]
	v_pk_add_f32 v[24:25], v[32:33], v[28:29]
	v_pk_mul_f32 v[28:29], v[20:21], v[20:21]
	v_pk_mul_f32 v[20:21], v[22:23], v[22:23]
	v_pk_mul_f32 v[30:31], v[18:19], v[18:19]
	v_pk_mul_f32 v[26:27], v[24:25], v[24:25]
	v_mov_b32_e32 v32, v20
	v_mov_b32_e32 v33, v30
	v_mov_b32_e32 v30, v21
	global_load_dwordx4 v[18:21], v88, s[8:9] offset:16
	global_load_dwordx4 v[22:25], v88, s[8:9]
	v_pk_add_f32 v[30:31], v[32:33], v[30:31]
	v_mov_b32_e32 v32, v26
	v_mov_b32_e32 v33, v28
	v_pk_add_f32 v[30:31], v[30:31], v[32:33]
	v_mov_b32_e32 v28, v27
	v_pk_add_f32 v[84:85], v[30:31], v[28:29]
	ds_read_b128 v[26:29], v89 offset:96
	ds_read_b128 v[30:33], v89 offset:112
	ds_read_b128 v[46:49], v74
	ds_read_b128 v[50:53], v74 offset:16
	global_load_dwordx4 v[54:57], v88, s[8:9] offset:48
	global_load_dwordx4 v[58:61], v88, s[8:9] offset:32
	v_add_u32_e32 v62, 0x10830, v89
	ds_read_b128 v[62:65], v62
	ds_read_b128 v[66:69], v89 offset:112
	s_waitcnt lgkmcnt(3)
	v_pk_add_f32 v[28:29], v[28:29], v[48:49]
	s_waitcnt lgkmcnt(2)
	v_pk_add_f32 v[30:31], v[30:31], v[50:51]
	v_pk_add_f32 v[26:27], v[26:27], v[46:47]
	v_pk_mul_f32 v[46:47], v[28:29], v[28:29]
	v_pk_mul_f32 v[26:27], v[26:27], v[26:27]
	v_pk_mul_f32 v[28:29], v[30:31], v[30:31]
	v_pk_add_f32 v[32:33], v[32:33], v[52:53]
	v_mov_b32_e32 v30, v26
	v_mov_b32_e32 v31, v28
	v_mov_b32_e32 v28, v27
	ds_read_b128 v[70:73], v89 offset:96
	ds_read_b128 v[74:77], v74
	v_pk_mul_f32 v[48:49], v[32:33], v[32:33]
	v_pk_add_f32 v[50:51], v[30:31], v[28:29]
	global_load_dwordx4 v[26:29], v88, s[8:9] offset:80
	global_load_dwordx4 v[30:33], v88, s[8:9] offset:64
	v_add_f32_e32 v12, v12, v13
	v_add_f32_e32 v12, v12, v82
	v_mov_b32_e32 v52, v46
	v_mov_b32_e32 v53, v48
	v_add_f32_e32 v12, v12, v83
	v_pk_add_f32 v[50:51], v[50:51], v[52:53]
	v_mov_b32_e32 v48, v47
	v_add_f32_e32 v12, v12, v84
	v_pk_add_f32 v[46:47], v[50:51], v[48:49]
	v_add_f32_e32 v12, v12, v85
	v_add_f32_e32 v12, v12, v46
	v_add_f32_e32 v12, v12, v47
	global_load_dwordx4 v[46:49], v88, s[8:9] offset:96
	global_load_dwordx4 v[50:53], v88, s[8:9] offset:112
	ds_bpermute_b32 v13, v181, v12
	s_mov_b32 s0, 0x800000
	v_pk_add_f32 v[4:5], v[4:5], v[14:15]
	s_waitcnt lgkmcnt(4)
	v_pk_add_f32 v[0:1], v[0:1], v[62:63]
	s_waitcnt lgkmcnt(0)
	v_add_f32_e32 v12, v12, v13
	ds_bpermute_b32 v13, v180, v12
	s_waitcnt lgkmcnt(0)
	v_add_f32_e32 v12, v12, v13
	v_mov_b32_e32 v13, 0x3727c5ac
	v_fmac_f32_e32 v13, 0x3c000000, v12
	v_mul_f32_e32 v12, 0x4b800000, v13
	v_cmp_gt_f32_e32 vcc, s0, v13
	s_lshl_b32 s0, s12, 1
	s_nop 0
	v_cndmask_b32_e32 v12, v13, v12, vcc
	v_rsq_f32_e32 v12, v12
	s_nop 0
	v_mul_f32_e32 v13, 0x45800000, v12
	v_cndmask_b32_e32 v12, v12, v13, vcc
	v_mul_f32_e32 v82, 0x3f4ccccd, v12
	v_add_u32_e32 v12, s16, v86
	v_mov_b32_e32 v13, 0
	v_lshlrev_b64 v[84:85], 12, v[12:13]
	v_lshl_add_u64 v[84:85], s[6:7], 0, v[84:85]
	v_pk_mul_f32 v[4:5], v[82:83], v[4:5] op_sel_hi:[0,1]
	v_lshl_add_u64 v[84:85], v[84:85], 0, s[0:1]
	v_lshlrev_b32_e32 v12, 1, v87
	v_lshl_add_u64 v[84:85], v[84:85], 0, v[12:13]
	v_pk_mul_f32 v[0:1], v[82:83], v[0:1] op_sel_hi:[0,1]
	v_pk_mul_f32 v[10:11], v[82:83], v[10:11] op_sel_hi:[0,1]
	v_pk_mul_f32 v[8:9], v[82:83], v[8:9] op_sel_hi:[0,1]
	s_waitcnt vmcnt(7)
	v_pk_mul_f32 v[4:5], v[4:5], v[18:19]
	s_nop 0
	v_cvt_pk_f16_f32 v12, v4, v5
	v_pk_add_f32 v[4:5], v[6:7], v[16:17]
	v_pk_mul_f32 v[6:7], v[82:83], v[78:79] op_sel_hi:[0,1]
	v_pk_mul_f32 v[4:5], v[82:83], v[4:5] op_sel_hi:[0,1]
	v_pk_mul_f32 v[4:5], v[4:5], v[20:21]
	s_waitcnt vmcnt(6)
	v_pk_mul_f32 v[10:11], v[10:11], v[22:23]
	v_cvt_pk_f16_f32 v13, v4, v5
	v_pk_mul_f32 v[4:5], v[82:83], v[80:81] op_sel_hi:[0,1]
	s_waitcnt vmcnt(4)
	v_pk_mul_f32 v[4:5], v[4:5], v[58:59]
	v_pk_mul_f32 v[6:7], v[6:7], v[60:61]
	v_pk_mul_f32 v[0:1], v[0:1], v[54:55]
	v_cvt_pk_f16_f32 v4, v4, v5
	v_cvt_pk_f16_f32 v5, v6, v7
	v_cvt_pk_f16_f32 v6, v0, v1
	v_pk_add_f32 v[0:1], v[2:3], v[64:65]
	v_pk_add_f32 v[2:3], v[44:45], v[40:41]
	v_pk_mul_f32 v[0:1], v[82:83], v[0:1] op_sel_hi:[0,1]
	v_pk_mul_f32 v[0:1], v[0:1], v[56:57]
	v_pk_mul_f32 v[8:9], v[8:9], v[24:25]
	v_cvt_pk_f16_f32 v7, v0, v1
	global_store_dwordx4 v[84:85], v[4:7], off offset:16
	v_pk_add_f32 v[0:1], v[42:43], v[38:39]
	v_cvt_pk_f16_f32 v10, v10, v11
	v_add_u32_e32 v4, 0x10850, v89
	v_pk_mul_f32 v[6:7], v[82:83], v[2:3] op_sel_hi:[0,1]
	ds_read_b128 v[2:5], v4
	v_pk_mul_f32 v[0:1], v[82:83], v[0:1] op_sel_hi:[0,1]
	s_waitcnt vmcnt(3)
	v_pk_mul_f32 v[0:1], v[0:1], v[30:31]
	v_pk_mul_f32 v[6:7], v[6:7], v[32:33]
	v_cvt_pk_f16_f32 v0, v0, v1
	v_cvt_pk_f16_f32 v1, v6, v7
	v_add_u32_e32 v6, 0x10870, v89
	v_cvt_pk_f16_f32 v11, v8, v9
	ds_read_b128 v[6:9], v6
	s_waitcnt lgkmcnt(1)
	v_pk_add_f32 v[2:3], v[34:35], v[2:3]
	v_pk_add_f32 v[4:5], v[36:37], v[4:5]
	v_pk_mul_f32 v[2:3], v[82:83], v[2:3] op_sel_hi:[0,1]
	v_pk_mul_f32 v[4:5], v[82:83], v[4:5] op_sel_hi:[0,1]
	v_pk_mul_f32 v[2:3], v[2:3], v[26:27]
	v_pk_mul_f32 v[4:5], v[4:5], v[28:29]
	v_cvt_pk_f16_f32 v2, v2, v3
	v_cvt_pk_f16_f32 v3, v4, v5
	global_store_dwordx4 v[84:85], v[0:3], off offset:32
	s_waitcnt lgkmcnt(0)
	v_pk_add_f32 v[4:5], v[68:69], v[8:9]
	global_store_dwordx4 v[84:85], v[10:13], off
	v_pk_add_f32 v[0:1], v[70:71], v[74:75]
	v_pk_add_f32 v[2:3], v[72:73], v[76:77]
	v_pk_mul_f32 v[0:1], v[82:83], v[0:1] op_sel_hi:[0,1]
	v_pk_mul_f32 v[2:3], v[82:83], v[2:3] op_sel_hi:[0,1]
	s_waitcnt vmcnt(4)
	v_pk_mul_f32 v[0:1], v[0:1], v[46:47]
	v_pk_mul_f32 v[2:3], v[2:3], v[48:49]
	v_cvt_pk_f16_f32 v0, v0, v1
	v_cvt_pk_f16_f32 v1, v2, v3
	v_pk_add_f32 v[2:3], v[66:67], v[6:7]
	v_pk_mul_f32 v[4:5], v[82:83], v[4:5] op_sel_hi:[0,1]
	v_pk_mul_f32 v[2:3], v[82:83], v[2:3] op_sel_hi:[0,1]
	s_waitcnt vmcnt(3)
	v_pk_mul_f32 v[2:3], v[2:3], v[50:51]
	v_pk_mul_f32 v[4:5], v[4:5], v[52:53]
	v_cvt_pk_f16_f32 v2, v2, v3
	v_cvt_pk_f16_f32 v3, v4, v5
	global_store_dwordx4 v[84:85], v[0:3], off offset:48
	s_endpgm
